# speedup vs baseline: 1.0765x; 1.0146x over previous
_Z6scan_kPKDF16_S0_S0_S0_PKfPf:
	s_load_dwordx8 s[4:11], s[0:1], 0x0
	s_load_dwordx4 s[12:15], s[0:1], 0x20
	v_and_b32_e32 v1, 63, v0
	v_lshrrev_b32_e32 v2, 6, v0
	s_nop 1
	v_readfirstlane_b32 s16, v2
	s_lshr_b32 s17, s2, 7
	s_and_b32 s18, s2, 127
	s_lshl_b32 s18, s18, 2
	s_add_u32 s18, s18, s16
	s_lshl_b32 s19, s17, 9
	s_add_u32 s19, s19, s18
	s_mul_i32 s28, s16, 4608
	s_add_u32 s28, s28, 67584
	s_lshl_b32 s32, s16, 10
	s_add_u32 s33, s32, 0x1000
	s_add_u32 s34, s32, 0x2000
	s_add_u32 s35, s32, 0x3000
	s_mov_b32 s46, 0x200
	s_mov_b32 s47, 0
	s_mov_b32 s40, 0
	v_lshlrev_b32_e32 v2, 4, v1
	v_add_u32_e32 v3, 0x1000, v2
	v_add_u32_e32 v4, 0x2000, v2
	v_add_u32_e32 v5, 0x3000, v2
	v_lshlrev_b32_e32 v6, 2, v1
	v_lshlrev_b32_e32 v7, 1, v1
	v_and_b32_e32 v20, 7, v1
	v_lshlrev_b32_e32 v20, 1, v20
	v_add_u32_e32 v8, v2, v20
	v_add_u32_e32 v8, s28, v8
	v_and_b32_e32 v20, 3, v1
	v_bfe_u32 v21, v1, 3, 2
	v_lshl_add_u32 v20, v21, 2, v20
	v_lshrrev_b32_e32 v21, 5, v1
	v_bfe_u32 v22, v1, 2, 1
	v_bfe_u32 v23, v1, 4, 1
	v_cmp_eq_u32_e64 s[48:49], v21, v22
	v_cmp_eq_u32_e64 s[50:51], 0, v23
	s_nop 1
	s_and_b64 s[52:53], s[48:49], s[50:51]
	s_andn2_b64 s[54:55], s[48:49], s[50:51]
	v_mov_b32_e32 v24, 65536
	v_lshlrev_b32_e32 v25, 1, v20
	v_add_u32_e32 v25, s28, v25
	v_add_u32_e32 v26, 0x100, v25
	s_nop 1
	v_cndmask_b32_e64 v9, v24, v25, s[48:49]
	v_cndmask_b32_e64 v10, v24, v26, s[48:49]
	v_lshlrev_b32_e32 v25, 4, v20
	v_add_u32_e32 v25, s28, v25
	v_add_u32_e32 v25, 0x200, v25
	v_add_u32_e32 v26, 0x800, v25
	v_cndmask_b32_e64 v11, v24, v25, s[48:49]
	v_cndmask_b32_e64 v13, v24, v26, s[48:49]
	v_mov_b32_e32 v15, 1.0
	v_and_b32_e32 v89, 15, v1
	v_cmp_eq_u32_e64 s[42:43], 0, v89
	s_waitcnt lgkmcnt(0)
	s_lshl_b32 s30, s19, 13
	s_add_u32 s24, s4, s30
	s_addc_u32 s25, s5, 0
	s_add_u32 s26, s6, s30
	s_addc_u32 s27, s7, 0
	s_lshl_b32 s30, s17, 19
	s_add_u32 s30, s30, s32
	s_add_u32 s20, s8, s30
	s_addc_u32 s21, s9, 0
	s_add_u32 s22, s10, s30
	s_addc_u32 s23, s11, 0
	s_lshl_b32 s30, s18, 8
	s_add_u32 s12, s12, s30
	s_addc_u32 s13, s13, 0
	global_load_dword v90, v6, s[12:13]
	global_load_ushort v18, v7, s[26:27]
	global_load_ushort v19, v7, s[26:27] offset:128
	s_lshl_b32 s30, s19, 14
	s_add_u32 s14, s14, s30
	s_addc_u32 s15, s15, 0
	v_and_b32_e32 v30, 48, v1
	v_mov_b32_e32 v31, 0
	v_lshl_add_u64 v[16:17], s[14:15], 0, v[30:31]
	v_mov_b32_e32 v36, 0
	v_mov_b32_e32 v37, 0
	v_mov_b32_e32 v38, 0
	v_mov_b32_e32 v39, 0
	v_add_u32_e32 v29, 65536, v2
	ds_write_b128 v29, v[36:39]
	ds_write_b128 v29, v[36:39] offset:1024
	v_add_u32_e32 v29, s28, v2
	ds_write_b128 v29, v[36:39] offset:512
	ds_write_b128 v29, v[36:39] offset:1536
	ds_write_b128 v29, v[36:39] offset:2560
	ds_write_b128 v29, v[36:39] offset:3584
	s_mov_b32 m0, s32
	s_nop 0
	global_load_lds_dwordx4 v2, s[20:21]
	s_add_i32 m0, s32, 32768
	s_nop 0
	global_load_lds_dwordx4 v2, s[22:23]
	s_mov_b32 m0, s33
	s_nop 0
	global_load_lds_dwordx4 v3, s[20:21]
	s_add_i32 m0, s33, 32768
	s_nop 0
	global_load_lds_dwordx4 v3, s[22:23]
	s_mov_b32 m0, s34
	s_nop 0
	global_load_lds_dwordx4 v4, s[20:21]
	s_add_i32 m0, s34, 32768
	s_nop 0
	global_load_lds_dwordx4 v4, s[22:23]
	s_mov_b32 m0, s35
	s_nop 0
	global_load_lds_dwordx4 v5, s[20:21]
	s_add_i32 m0, s35, 32768
	s_nop 0
	global_load_lds_dwordx4 v5, s[22:23]
	s_mov_b32 m0, s28
	s_nop 0
	global_load_lds_dword v6, s[24:25]
	s_add_u32 s20, s20, 0x4000
	s_addc_u32 s21, s21, 0
	s_add_u32 s22, s22, 0x4000
	s_addc_u32 s23, s23, 0
	s_add_u32 s24, s24, 0x100
	s_addc_u32 s25, s25, 0
	s_add_i32 m0, s32, 0x4000
	s_nop 0
	global_load_lds_dwordx4 v2, s[20:21]
	s_add_i32 m0, s32, 49152
	s_nop 0
	global_load_lds_dwordx4 v2, s[22:23]
	s_add_i32 m0, s33, 0x4000
	s_nop 0
	global_load_lds_dwordx4 v3, s[20:21]
	s_add_i32 m0, s33, 49152
	s_nop 0
	global_load_lds_dwordx4 v3, s[22:23]
	s_add_i32 m0, s34, 0x4000
	s_nop 0
	global_load_lds_dwordx4 v4, s[20:21]
	s_add_i32 m0, s34, 49152
	s_nop 0
	global_load_lds_dwordx4 v4, s[22:23]
	s_add_i32 m0, s35, 0x4000
	s_nop 0
	global_load_lds_dwordx4 v5, s[20:21]
	s_add_i32 m0, s35, 49152
	s_nop 0
	global_load_lds_dwordx4 v5, s[22:23]
	s_add_i32 m0, s28, 0x100
	s_nop 0
	global_load_lds_dword v6, s[24:25]
	s_add_u32 s20, s20, 0x4000
	s_addc_u32 s21, s21, 0
	s_add_u32 s22, s22, 0x4000
	s_addc_u32 s23, s23, 0
	s_add_u32 s24, s24, 0x100
	s_addc_u32 s25, s25, 0
	s_mov_b32 s3, 0x3fb8aa3b
	s_waitcnt vmcnt(20)
	v_mul_f32_e32 v91, 0x3fb8aa3b, v90
	v_fma_f32 v92, v90, s3, -v91
	v_rndne_f32_e32 v93, v91
	v_fmamk_f32 v92, v90, 0x32a5705f, v92
	v_sub_f32_e32 v91, v91, v93
	v_add_f32_e32 v91, v91, v92
	v_exp_f32_e32 v91, v91
	v_cvt_i32_f32_e32 v92, v93
	s_mov_b32 s3, 0xc2ce8ed0
	v_cmp_ngt_f32_e32 vcc, s3, v90
	s_mov_b32 s3, 0x42b17218
	v_ldexp_f32 v91, v91, v92
	v_cndmask_b32_e32 v91, 0, v91, vcc
	v_mov_b32_e32 v92, 0x7f800000
	v_cmp_nlt_f32_e32 vcc, s3, v90
	s_mov_b32 s3, 0xbfb8aa3b
	s_nop 1
	v_cndmask_b32_e32 v90, v92, v91, vcc
	v_mov_b32_e32 v93, 0
	s_nop 0
	v_fma_mixlo_f16 v93, v90, s3, 0
	v_and_b32_e32 v28, 0xffff, v93
	v_mov_b32_e32 v29, 0
	v_mov_b32_e32 v30, 0
	v_mov_b32_e32 v31, 0
	v_mov_b32_e32 v32, 0
	v_mov_b32_e32 v33, 0
	v_mov_b32_e32 v34, 0
	v_mov_b32_e32 v35, 0
	v_mov_b32_e32 v94, 0x1c00
	v_mov_b32_e32 v95, 0x1c000000
	v_cmp_eq_u32_e32 vcc, 0, v89
	s_nop 1
	v_cndmask_b32_e32 v20, 0, v94, vcc
	v_cmp_eq_u32_e32 vcc, 1, v89
	s_nop 1
	v_cndmask_b32_e32 v20, v20, v95, vcc
	v_cmp_eq_u32_e32 vcc, 2, v89
	s_nop 1
	v_cndmask_b32_e32 v21, 0, v94, vcc
	v_cmp_eq_u32_e32 vcc, 3, v89
	s_nop 1
	v_cndmask_b32_e32 v21, v21, v95, vcc
	v_cmp_eq_u32_e32 vcc, 4, v89
	s_nop 1
	v_cndmask_b32_e32 v22, 0, v94, vcc
	v_cmp_eq_u32_e32 vcc, 5, v89
	s_nop 1
	v_cndmask_b32_e32 v22, v22, v95, vcc
	v_cmp_eq_u32_e32 vcc, 6, v89
	s_nop 1
	v_cndmask_b32_e32 v23, 0, v94, vcc
	v_cmp_eq_u32_e32 vcc, 7, v89
	s_nop 1
	v_cndmask_b32_e32 v23, v23, v95, vcc
	v_cmp_eq_u32_e32 vcc, 8, v89
	s_nop 1
	v_cndmask_b32_e32 v24, 0, v94, vcc
	v_cmp_eq_u32_e32 vcc, 9, v89
	s_nop 1
	v_cndmask_b32_e32 v24, v24, v95, vcc
	v_cmp_eq_u32_e32 vcc, 10, v89
	s_nop 1
	v_cndmask_b32_e32 v25, 0, v94, vcc
	v_cmp_eq_u32_e32 vcc, 11, v89
	s_nop 1
	v_cndmask_b32_e32 v25, v25, v95, vcc
	v_cmp_eq_u32_e32 vcc, 12, v89
	s_nop 1
	v_cndmask_b32_e32 v26, 0, v94, vcc
	v_cmp_eq_u32_e32 vcc, 13, v89
	s_nop 1
	v_cndmask_b32_e32 v26, v26, v95, vcc
	v_cmp_eq_u32_e32 vcc, 14, v89
	s_nop 1
	v_cndmask_b32_e32 v27, 0, v94, vcc
	v_cmp_eq_u32_e32 vcc, 15, v89
	s_nop 1
	v_cndmask_b32_e32 v27, v27, v95, vcc
	v_mov_b32_e32 v191, 0
	v_mov_b32_e32 v68, 0
	v_mov_b32_e32 v69, 0
	v_mov_b32_e32 v70, 0
	v_mov_b32_e32 v71, 0
	v_mov_b32_e32 v72, 0
	v_mov_b32_e32 v73, 0
	v_mov_b32_e32 v74, 0
	v_mov_b32_e32 v75, 0
	v_mov_b32_e32 v76, 0
	v_mov_b32_e32 v77, 0
	v_mov_b32_e32 v78, 0
	v_mov_b32_e32 v79, 0
	v_mov_b32_e32 v80, 0
	v_mov_b32_e32 v81, 0
	v_mov_b32_e32 v82, 0
	v_mov_b32_e32 v83, 0
	s_waitcnt vmcnt(18)
	ds_write_b16 v8, v18 offset:512
	ds_write_b16 v8, v19 offset:1536
	s_add_u32 s26, s26, 0x100
	s_addc_u32 s27, s27, 0
	global_load_ushort v18, v7, s[26:27]
	global_load_ushort v19, v7, s[26:27] offset:128
	s_add_u32 s26, s26, 0x100
	s_addc_u32 s27, s27, 0
	s_waitcnt vmcnt(0)
	s_waitcnt lgkmcnt(0)
	s_barrier
	ds_read_b128 v[52:55], v2 offset:32768
	ds_read_b128 v[56:59], v2 offset:33792
	ds_read_u16 v32, v9 offset:0
	ds_read_b128 v[36:39], v11 offset:0
	ds_read_b128 v[44:47], v2 offset:0
	ds_read_b128 v[48:51], v2 offset:1024
	s_waitcnt lgkmcnt(0)
	v_mfma_f32_32x32x16_f16 v[96:111], v[32:35], v[28:31], 0
	v_mfma_f32_32x32x16_f16 v[128:143], v[36:39], v[44:47], 0
	v_mfma_f32_32x32x16_f16 v[160:175], v[36:39], v[48:51], 0
	ds_read_u16 v32, v9 offset:32
	ds_read_b128 v[36:39], v11 offset:256
	ds_read_b128 v[44:47], v2 offset:2048
	ds_read_b128 v[48:51], v2 offset:3072
	s_nop 15
	s_nop 15
.Lscan_loop:
	v_exp_f32_e32 v96, v96
	v_exp_f32_e32 v97, v97
	v_mfma_f32_16x16x32_f16 v[80:83], v[72:75], v[24:27], v[80:83]
	ds_read_b128 v[60:63], v2 offset:34816
	v_exp_f32_e32 v98, v98
	v_exp_f32_e32 v99, v99
	s_waitcnt lgkmcnt(1)
	v_mfma_f32_32x32x16_f16 v[112:127], v[32:35], v[28:31], 0
	ds_read_u16 v32, v9 offset:64
	ds_read_b128 v[64:67], v2 offset:35840
	v_fmac_f32_e32 v128, v96, v191
	v_exp_f32_e32 v100, v100
	v_fmac_f32_e32 v129, v97, v128
	v_exp_f32_e32 v101, v101
	v_fmac_f32_e32 v130, v98, v129
	v_cvt_pkrtz_f16_f32 v68, v128, v129
	v_exp_f32_e32 v102, v102
	v_fmac_f32_e32 v131, v99, v130
	v_pk_mul_f16 v68, v52, v68
	v_exp_f32_e32 v103, v103
	v_mfma_f32_32x32x16_f16 v[144:159], v[36:39], v[44:47], 0
	ds_read_b128 v[44:47], v2 offset:4096
	v_fmac_f32_e32 v132, v100, v131
	v_cvt_pkrtz_f16_f32 v69, v130, v131
	v_exp_f32_e32 v104, v104
	v_fmac_f32_e32 v133, v101, v132
	v_pk_mul_f16 v69, v53, v69
	v_exp_f32_e32 v105, v105
	v_fmac_f32_e32 v134, v102, v133
	v_cvt_pkrtz_f16_f32 v70, v132, v133
	v_exp_f32_e32 v106, v106
	v_fmac_f32_e32 v135, v103, v134
	v_pk_mul_f16 v70, v54, v70
	v_exp_f32_e32 v107, v107
	v_mfma_f32_32x32x16_f16 v[176:191], v[36:39], v[48:51], 0
	ds_read_b128 v[36:39], v11 offset:512
	ds_read_b128 v[48:51], v2 offset:5120
	v_cvt_pkrtz_f16_f32 v71, v134, v135
	v_fmac_f32_e32 v168, v104, v135
	v_pk_mul_f16 v71, v55, v71
	v_exp_f32_e32 v108, v108
	v_fmac_f32_e32 v169, v105, v168
	v_mfma_f32_16x16x32_f16 v[76:79], v[68:71], v[20:23], 0
	v_cvt_pkrtz_f16_f32 v72, v168, v169
	v_exp_f32_e32 v109, v109
	v_fmac_f32_e32 v170, v106, v169
	v_pk_mul_f16 v72, v56, v72
	v_add_f32_e32 v84, v80, v81
	v_fmac_f32_e32 v171, v107, v170
	v_exp_f32_e32 v110, v110
	v_cvt_pkrtz_f16_f32 v73, v170, v171
	v_fmac_f32_e32 v172, v108, v171
	v_pk_mul_f16 v73, v57, v73
	v_add_f32_e32 v85, v82, v83
	v_fmac_f32_e32 v173, v109, v172
	v_exp_f32_e32 v111, v111
	v_cvt_pkrtz_f16_f32 v74, v172, v173
	v_fmac_f32_e32 v174, v110, v173
	v_add_f32_e32 v84, v84, v85
	v_fmac_f32_e32 v175, v111, v174
	v_pk_mul_f16 v74, v58, v74
	v_cvt_pkrtz_f16_f32 v75, v174, v175
	v_mfma_f32_16x16x4_f32 a[28:31], v84, v15, 0
	v_pk_mul_f16 v75, v59, v75
	v_exp_f32_e32 v112, v112
	v_exp_f32_e32 v113, v113
	v_mfma_f32_16x16x32_f16 v[76:79], v[72:75], v[24:27], v[76:79]
	ds_read_b128 v[52:55], v2 offset:36864
	v_exp_f32_e32 v114, v114
	v_exp_f32_e32 v115, v115
	s_waitcnt lgkmcnt(1)
	v_mfma_f32_32x32x16_f16 v[96:111], v[32:35], v[28:31], 0
	ds_read_u16 v32, v9 offset:96
	ds_read_b128 v[56:59], v2 offset:37888
	v_fmac_f32_e32 v144, v112, v175
	v_exp_f32_e32 v116, v116
	v_fmac_f32_e32 v145, v113, v144
	v_exp_f32_e32 v117, v117
	v_fmac_f32_e32 v146, v114, v145
	v_cvt_pkrtz_f16_f32 v68, v144, v145
	v_exp_f32_e32 v118, v118
	v_fmac_f32_e32 v147, v115, v146
	v_pk_mul_f16 v68, v60, v68
	v_exp_f32_e32 v119, v119
	v_mfma_f32_32x32x16_f16 v[128:143], v[36:39], v[44:47], 0
	ds_read_b128 v[44:47], v2 offset:6144
	v_fmac_f32_e32 v148, v116, v147
	v_cvt_pkrtz_f16_f32 v69, v146, v147
	v_exp_f32_e32 v120, v120
	v_fmac_f32_e32 v149, v117, v148
	v_pk_mul_f16 v69, v61, v69
	v_exp_f32_e32 v121, v121
	v_fmac_f32_e32 v150, v118, v149
	v_cvt_pkrtz_f16_f32 v70, v148, v149
	v_exp_f32_e32 v122, v122
	v_fmac_f32_e32 v151, v119, v150
	v_pk_mul_f16 v70, v62, v70
	v_exp_f32_e32 v123, v123
	v_mfma_f32_32x32x16_f16 v[160:175], v[36:39], v[48:51], 0
	ds_read_b128 v[36:39], v11 offset:768
	ds_read_b128 v[48:51], v2 offset:7168
	v_cvt_pkrtz_f16_f32 v71, v150, v151
	v_fmac_f32_e32 v184, v120, v151
	v_pk_mul_f16 v71, v63, v71
	v_exp_f32_e32 v124, v124
	v_fmac_f32_e32 v185, v121, v184
	v_mfma_f32_16x16x32_f16 v[80:83], v[68:71], v[20:23], 0
	v_cvt_pkrtz_f16_f32 v72, v184, v185
	v_exp_f32_e32 v125, v125
	v_fmac_f32_e32 v186, v122, v185
	v_pk_mul_f16 v72, v64, v72
	v_add_f32_e32 v84, v76, v77
	v_fmac_f32_e32 v187, v123, v186
	v_exp_f32_e32 v126, v126
	v_cvt_pkrtz_f16_f32 v73, v186, v187
	v_fmac_f32_e32 v188, v124, v187
	v_pk_mul_f16 v73, v65, v73
	v_add_f32_e32 v85, v78, v79
	v_fmac_f32_e32 v189, v125, v188
	v_exp_f32_e32 v127, v127
	v_cvt_pkrtz_f16_f32 v74, v188, v189
	v_fmac_f32_e32 v190, v126, v189
	v_add_f32_e32 v84, v84, v85
	v_fmac_f32_e32 v191, v127, v190
	v_pk_mul_f16 v74, v66, v74
	v_cvt_pkrtz_f16_f32 v75, v190, v191
	v_mfma_f32_16x16x4_f32 a[0:3], v84, v15, 0
	v_pk_mul_f16 v75, v67, v75
	v_exp_f32_e32 v96, v96
	v_exp_f32_e32 v97, v97
	v_mfma_f32_16x16x32_f16 v[80:83], v[72:75], v[24:27], v[80:83]
	ds_read_b128 v[60:63], v2 offset:38912
	v_exp_f32_e32 v98, v98
	v_exp_f32_e32 v99, v99
	s_waitcnt lgkmcnt(1)
	v_mfma_f32_32x32x16_f16 v[112:127], v[32:35], v[28:31], 0
	ds_read_u16 v32, v9 offset:128
	ds_read_b128 v[64:67], v2 offset:39936
	v_fmac_f32_e32 v128, v96, v191
	v_exp_f32_e32 v100, v100
	v_fmac_f32_e32 v129, v97, v128
	v_exp_f32_e32 v101, v101
	v_fmac_f32_e32 v130, v98, v129
	v_cvt_pkrtz_f16_f32 v68, v128, v129
	v_exp_f32_e32 v102, v102
	v_fmac_f32_e32 v131, v99, v130
	v_pk_mul_f16 v68, v52, v68
	v_exp_f32_e32 v103, v103
	v_mfma_f32_32x32x16_f16 v[144:159], v[36:39], v[44:47], 0
	ds_read_b128 v[44:47], v2 offset:8192
	v_fmac_f32_e32 v132, v100, v131
	v_cvt_pkrtz_f16_f32 v69, v130, v131
	v_exp_f32_e32 v104, v104
	v_fmac_f32_e32 v133, v101, v132
	v_pk_mul_f16 v69, v53, v69
	v_exp_f32_e32 v105, v105
	v_fmac_f32_e32 v134, v102, v133
	v_cvt_pkrtz_f16_f32 v70, v132, v133
	v_exp_f32_e32 v106, v106
	v_fmac_f32_e32 v135, v103, v134
	v_pk_mul_f16 v70, v54, v70
	v_exp_f32_e32 v107, v107
	v_mfma_f32_32x32x16_f16 v[176:191], v[36:39], v[48:51], 0
	ds_read_b128 v[36:39], v11 offset:1024
	ds_read_b128 v[48:51], v2 offset:9216
	v_cvt_pkrtz_f16_f32 v71, v134, v135
	v_fmac_f32_e32 v168, v104, v135
	v_pk_mul_f16 v71, v55, v71
	v_exp_f32_e32 v108, v108
	v_fmac_f32_e32 v169, v105, v168
	v_mfma_f32_16x16x32_f16 v[76:79], v[68:71], v[20:23], 0
	v_cvt_pkrtz_f16_f32 v72, v168, v169
	v_exp_f32_e32 v109, v109
	v_fmac_f32_e32 v170, v106, v169
	v_pk_mul_f16 v72, v56, v72
	v_add_f32_e32 v84, v80, v81
	v_fmac_f32_e32 v171, v107, v170
	v_exp_f32_e32 v110, v110
	v_cvt_pkrtz_f16_f32 v73, v170, v171
	v_fmac_f32_e32 v172, v108, v171
	v_pk_mul_f16 v73, v57, v73
	v_add_f32_e32 v85, v82, v83
	v_fmac_f32_e32 v173, v109, v172
	v_exp_f32_e32 v111, v111
	v_cvt_pkrtz_f16_f32 v74, v172, v173
	v_fmac_f32_e32 v174, v110, v173
	v_add_f32_e32 v84, v84, v85
	v_fmac_f32_e32 v175, v111, v174
	v_pk_mul_f16 v74, v58, v74
	v_cvt_pkrtz_f16_f32 v75, v174, v175
	v_mfma_f32_16x16x4_f32 a[4:7], v84, v15, 0
	v_pk_mul_f16 v75, v59, v75
	v_exp_f32_e32 v112, v112
	v_exp_f32_e32 v113, v113
	v_mfma_f32_16x16x32_f16 v[76:79], v[72:75], v[24:27], v[76:79]
	ds_read_b128 v[52:55], v2 offset:40960
	v_exp_f32_e32 v114, v114
	v_exp_f32_e32 v115, v115
	s_waitcnt lgkmcnt(1)
	v_mfma_f32_32x32x16_f16 v[96:111], v[32:35], v[28:31], 0
	ds_read_u16 v32, v9 offset:160
	ds_read_b128 v[56:59], v2 offset:41984
	v_fmac_f32_e32 v144, v112, v175
	v_exp_f32_e32 v116, v116
	v_fmac_f32_e32 v145, v113, v144
	v_exp_f32_e32 v117, v117
	v_fmac_f32_e32 v146, v114, v145
	v_cvt_pkrtz_f16_f32 v68, v144, v145
	v_exp_f32_e32 v118, v118
	v_fmac_f32_e32 v147, v115, v146
	v_pk_mul_f16 v68, v60, v68
	v_exp_f32_e32 v119, v119
	v_mfma_f32_32x32x16_f16 v[128:143], v[36:39], v[44:47], 0
	ds_read_b128 v[44:47], v2 offset:10240
	v_fmac_f32_e32 v148, v116, v147
	v_cvt_pkrtz_f16_f32 v69, v146, v147
	v_exp_f32_e32 v120, v120
	v_fmac_f32_e32 v149, v117, v148
	v_pk_mul_f16 v69, v61, v69
	v_exp_f32_e32 v121, v121
	v_fmac_f32_e32 v150, v118, v149
	v_cvt_pkrtz_f16_f32 v70, v148, v149
	v_exp_f32_e32 v122, v122
	v_fmac_f32_e32 v151, v119, v150
	v_pk_mul_f16 v70, v62, v70
	v_exp_f32_e32 v123, v123
	v_mfma_f32_32x32x16_f16 v[160:175], v[36:39], v[48:51], 0
	ds_read_b128 v[36:39], v11 offset:1280
	ds_read_b128 v[48:51], v2 offset:11264
	v_cvt_pkrtz_f16_f32 v71, v150, v151
	v_fmac_f32_e32 v184, v120, v151
	v_pk_mul_f16 v71, v63, v71
	v_exp_f32_e32 v124, v124
	v_fmac_f32_e32 v185, v121, v184
	v_mfma_f32_16x16x32_f16 v[80:83], v[68:71], v[20:23], 0
	v_cvt_pkrtz_f16_f32 v72, v184, v185
	v_exp_f32_e32 v125, v125
	v_fmac_f32_e32 v186, v122, v185
	v_pk_mul_f16 v72, v64, v72
	v_add_f32_e32 v84, v76, v77
	v_fmac_f32_e32 v187, v123, v186
	v_exp_f32_e32 v126, v126
	v_cvt_pkrtz_f16_f32 v73, v186, v187
	v_fmac_f32_e32 v188, v124, v187
	v_pk_mul_f16 v73, v65, v73
	v_add_f32_e32 v85, v78, v79
	v_fmac_f32_e32 v189, v125, v188
	v_exp_f32_e32 v127, v127
	v_cvt_pkrtz_f16_f32 v74, v188, v189
	v_fmac_f32_e32 v190, v126, v189
	v_add_f32_e32 v84, v84, v85
	v_fmac_f32_e32 v191, v127, v190
	v_pk_mul_f16 v74, v66, v74
	v_cvt_pkrtz_f16_f32 v75, v190, v191
	v_mfma_f32_16x16x4_f32 a[8:11], v84, v15, 0
	v_pk_mul_f16 v75, v67, v75
	v_exp_f32_e32 v96, v96
	v_exp_f32_e32 v97, v97
	v_mfma_f32_16x16x32_f16 v[80:83], v[72:75], v[24:27], v[80:83]
	ds_read_b128 v[60:63], v2 offset:43008
	v_exp_f32_e32 v98, v98
	v_exp_f32_e32 v99, v99
	s_waitcnt lgkmcnt(1)
	v_mfma_f32_32x32x16_f16 v[112:127], v[32:35], v[28:31], 0
	ds_read_u16 v32, v9 offset:192
	ds_read_b128 v[64:67], v2 offset:44032
	v_fmac_f32_e32 v128, v96, v191
	v_exp_f32_e32 v100, v100
	v_fmac_f32_e32 v129, v97, v128
	v_exp_f32_e32 v101, v101
	v_fmac_f32_e32 v130, v98, v129
	v_cvt_pkrtz_f16_f32 v68, v128, v129
	v_exp_f32_e32 v102, v102
	v_fmac_f32_e32 v131, v99, v130
	v_pk_mul_f16 v68, v52, v68
	v_exp_f32_e32 v103, v103
	v_mfma_f32_32x32x16_f16 v[144:159], v[36:39], v[44:47], 0
	ds_read_b128 v[44:47], v2 offset:12288
	v_fmac_f32_e32 v132, v100, v131
	v_cvt_pkrtz_f16_f32 v69, v130, v131
	v_exp_f32_e32 v104, v104
	v_fmac_f32_e32 v133, v101, v132
	v_pk_mul_f16 v69, v53, v69
	v_exp_f32_e32 v105, v105
	v_fmac_f32_e32 v134, v102, v133
	v_cvt_pkrtz_f16_f32 v70, v132, v133
	v_exp_f32_e32 v106, v106
	v_fmac_f32_e32 v135, v103, v134
	v_pk_mul_f16 v70, v54, v70
	v_exp_f32_e32 v107, v107
	v_mfma_f32_32x32x16_f16 v[176:191], v[36:39], v[48:51], 0
	ds_read_b128 v[36:39], v11 offset:1536
	ds_read_b128 v[48:51], v2 offset:13312
	v_cvt_pkrtz_f16_f32 v71, v134, v135
	v_fmac_f32_e32 v168, v104, v135
	v_pk_mul_f16 v71, v55, v71
	v_exp_f32_e32 v108, v108
	v_fmac_f32_e32 v169, v105, v168
	v_mfma_f32_16x16x32_f16 v[76:79], v[68:71], v[20:23], 0
	v_cvt_pkrtz_f16_f32 v72, v168, v169
	v_exp_f32_e32 v109, v109
	v_fmac_f32_e32 v170, v106, v169
	v_pk_mul_f16 v72, v56, v72
	v_add_f32_e32 v84, v80, v81
	v_fmac_f32_e32 v171, v107, v170
	v_exp_f32_e32 v110, v110
	v_cvt_pkrtz_f16_f32 v73, v170, v171
	v_fmac_f32_e32 v172, v108, v171
	v_pk_mul_f16 v73, v57, v73
	v_add_f32_e32 v85, v82, v83
	v_fmac_f32_e32 v173, v109, v172
	v_exp_f32_e32 v111, v111
	v_cvt_pkrtz_f16_f32 v74, v172, v173
	v_fmac_f32_e32 v174, v110, v173
	v_add_f32_e32 v84, v84, v85
	v_fmac_f32_e32 v175, v111, v174
	v_pk_mul_f16 v74, v58, v74
	v_cvt_pkrtz_f16_f32 v75, v174, v175
	v_mfma_f32_16x16x4_f32 a[12:15], v84, v15, 0
	v_pk_mul_f16 v75, v59, v75
	v_exp_f32_e32 v112, v112
	v_exp_f32_e32 v113, v113
	v_mfma_f32_16x16x32_f16 v[76:79], v[72:75], v[24:27], v[76:79]
	ds_read_b128 v[52:55], v2 offset:45056
	v_exp_f32_e32 v114, v114
	v_exp_f32_e32 v115, v115
	s_waitcnt lgkmcnt(1)
	v_mfma_f32_32x32x16_f16 v[96:111], v[32:35], v[28:31], 0
	ds_read_u16 v32, v9 offset:224
	ds_read_b128 v[56:59], v2 offset:46080
	v_fmac_f32_e32 v144, v112, v175
	v_exp_f32_e32 v116, v116
	v_fmac_f32_e32 v145, v113, v144
	v_exp_f32_e32 v117, v117
	v_fmac_f32_e32 v146, v114, v145
	v_cvt_pkrtz_f16_f32 v68, v144, v145
	v_exp_f32_e32 v118, v118
	v_fmac_f32_e32 v147, v115, v146
	v_pk_mul_f16 v68, v60, v68
	v_exp_f32_e32 v119, v119
	v_mfma_f32_32x32x16_f16 v[128:143], v[36:39], v[44:47], 0
	ds_read_b128 v[44:47], v2 offset:14336
	v_fmac_f32_e32 v148, v116, v147
	v_cvt_pkrtz_f16_f32 v69, v146, v147
	v_exp_f32_e32 v120, v120
	v_fmac_f32_e32 v149, v117, v148
	v_pk_mul_f16 v69, v61, v69
	v_exp_f32_e32 v121, v121
	v_fmac_f32_e32 v150, v118, v149
	v_cvt_pkrtz_f16_f32 v70, v148, v149
	v_exp_f32_e32 v122, v122
	v_fmac_f32_e32 v151, v119, v150
	v_pk_mul_f16 v70, v62, v70
	v_exp_f32_e32 v123, v123
	v_mfma_f32_32x32x16_f16 v[160:175], v[36:39], v[48:51], 0
	ds_read_b128 v[36:39], v11 offset:1792
	ds_read_b128 v[48:51], v2 offset:15360
	v_cvt_pkrtz_f16_f32 v71, v150, v151
	v_fmac_f32_e32 v184, v120, v151
	v_pk_mul_f16 v71, v63, v71
	v_exp_f32_e32 v124, v124
	v_fmac_f32_e32 v185, v121, v184
	v_mfma_f32_16x16x32_f16 v[80:83], v[68:71], v[20:23], 0
	v_cvt_pkrtz_f16_f32 v72, v184, v185
	v_exp_f32_e32 v125, v125
	v_fmac_f32_e32 v186, v122, v185
	v_pk_mul_f16 v72, v64, v72
	v_add_f32_e32 v84, v76, v77
	v_fmac_f32_e32 v187, v123, v186
	v_exp_f32_e32 v126, v126
	v_cvt_pkrtz_f16_f32 v73, v186, v187
	v_fmac_f32_e32 v188, v124, v187
	v_pk_mul_f16 v73, v65, v73
	v_add_f32_e32 v85, v78, v79
	v_fmac_f32_e32 v189, v125, v188
	v_exp_f32_e32 v127, v127
	v_cvt_pkrtz_f16_f32 v74, v188, v189
	v_fmac_f32_e32 v190, v126, v189
	v_add_f32_e32 v84, v84, v85
	v_fmac_f32_e32 v191, v127, v190
	v_pk_mul_f16 v74, v66, v74
	v_cvt_pkrtz_f16_f32 v75, v190, v191
	v_mfma_f32_16x16x4_f32 a[16:19], v84, v15, 0
	v_pk_mul_f16 v75, v67, v75
	v_exp_f32_e32 v96, v96
	v_exp_f32_e32 v97, v97
	v_mfma_f32_16x16x32_f16 v[80:83], v[72:75], v[24:27], v[80:83]
	ds_read_b128 v[60:63], v2 offset:47104
	ds_read_b128 v[64:67], v2 offset:48128
	s_waitcnt vmcnt(0)
	ds_write_b16 v8, v18 offset:2560
	ds_write_b16 v8, v19 offset:3584
	s_waitcnt lgkmcnt(0)
	s_barrier
	s_cmp_ge_u32 s40, 15
	s_cbranch_scc1 .Lscan_nodma0
	s_mov_b32 m0, s32
	s_nop 0
	global_load_lds_dwordx4 v2, s[20:21]
	s_add_i32 m0, s32, 32768
	s_nop 0
	global_load_lds_dwordx4 v2, s[22:23]
	s_mov_b32 m0, s33
	s_nop 0
	global_load_lds_dwordx4 v3, s[20:21]
	s_add_i32 m0, s33, 32768
	s_nop 0
	global_load_lds_dwordx4 v3, s[22:23]
	s_mov_b32 m0, s34
	s_nop 0
	global_load_lds_dwordx4 v4, s[20:21]
	s_add_i32 m0, s34, 32768
	s_nop 0
	global_load_lds_dwordx4 v4, s[22:23]
	s_mov_b32 m0, s35
	s_nop 0
	global_load_lds_dwordx4 v5, s[20:21]
	s_add_i32 m0, s35, 32768
	s_nop 0
	global_load_lds_dwordx4 v5, s[22:23]
	s_mov_b32 m0, s28
	s_nop 0
	global_load_lds_dword v6, s[24:25]
	global_load_ushort v18, v7, s[26:27]
	global_load_ushort v19, v7, s[26:27] offset:128
	s_add_u32 s20, s20, 0x4000
	s_addc_u32 s21, s21, 0
	s_add_u32 s22, s22, 0x4000
	s_addc_u32 s23, s23, 0
	s_add_u32 s24, s24, 0x100
	s_addc_u32 s25, s25, 0
	s_add_u32 s26, s26, 0x100
	s_addc_u32 s27, s27, 0

.Lscan_nocarry:
	global_store_dwordx4 v[16:17], a[0:3], off
	global_store_dwordx4 v[16:17], a[4:7], off offset:64
	global_store_dwordx4 v[16:17], a[8:11], off offset:128
	global_store_dwordx4 v[16:17], a[12:15], off offset:192
	global_store_dwordx4 v[16:17], a[16:19], off offset:256
	s_mov_b64 exec, s[44:45]
	v_lshl_add_u64 v[16:17], v[16:17], 0, s[46:47]
	v_exp_f32_e32 v98, v98
	v_exp_f32_e32 v99, v99
	s_waitcnt lgkmcnt(1)
	v_mfma_f32_32x32x16_f16 v[112:127], v[32:35], v[28:31], 0
	ds_read_u16 v32, v10 offset:0
	v_fmac_f32_e32 v128, v96, v191
	v_exp_f32_e32 v100, v100
	v_fmac_f32_e32 v129, v97, v128
	v_exp_f32_e32 v101, v101
	v_fmac_f32_e32 v130, v98, v129
	v_cvt_pkrtz_f16_f32 v68, v128, v129
	v_exp_f32_e32 v102, v102
	v_fmac_f32_e32 v131, v99, v130
	v_pk_mul_f16 v68, v52, v68
	v_exp_f32_e32 v103, v103
	v_mfma_f32_32x32x16_f16 v[144:159], v[36:39], v[44:47], 0
	ds_read_b128 v[44:47], v2 offset:16384
	v_fmac_f32_e32 v132, v100, v131
	v_cvt_pkrtz_f16_f32 v69, v130, v131
	v_exp_f32_e32 v104, v104
	v_fmac_f32_e32 v133, v101, v132
	v_pk_mul_f16 v69, v53, v69
	v_exp_f32_e32 v105, v105
	v_fmac_f32_e32 v134, v102, v133
	v_cvt_pkrtz_f16_f32 v70, v132, v133
	v_exp_f32_e32 v106, v106
	v_fmac_f32_e32 v135, v103, v134
	v_pk_mul_f16 v70, v54, v70
	v_exp_f32_e32 v107, v107
	v_mfma_f32_32x32x16_f16 v[176:191], v[36:39], v[48:51], 0
	ds_read_b128 v[36:39], v13 offset:0
	ds_read_b128 v[48:51], v2 offset:17408
	v_cvt_pkrtz_f16_f32 v71, v134, v135
	v_fmac_f32_e32 v168, v104, v135
	v_pk_mul_f16 v71, v55, v71
	v_exp_f32_e32 v108, v108
	v_fmac_f32_e32 v169, v105, v168
	v_mfma_f32_16x16x32_f16 v[76:79], v[68:71], v[20:23], 0
	v_cvt_pkrtz_f16_f32 v72, v168, v169
	v_exp_f32_e32 v109, v109
	v_fmac_f32_e32 v170, v106, v169
	v_pk_mul_f16 v72, v56, v72
	v_add_f32_e32 v84, v80, v81
	v_fmac_f32_e32 v171, v107, v170
	v_exp_f32_e32 v110, v110
	v_cvt_pkrtz_f16_f32 v73, v170, v171
	v_fmac_f32_e32 v172, v108, v171
	v_pk_mul_f16 v73, v57, v73
	v_add_f32_e32 v85, v82, v83
	v_fmac_f32_e32 v173, v109, v172
	v_exp_f32_e32 v111, v111
	v_cvt_pkrtz_f16_f32 v74, v172, v173
	v_fmac_f32_e32 v174, v110, v173
	v_add_f32_e32 v84, v84, v85
	v_fmac_f32_e32 v175, v111, v174
	v_pk_mul_f16 v74, v58, v74
	v_cvt_pkrtz_f16_f32 v75, v174, v175
	v_mfma_f32_16x16x4_f32 a[20:23], v84, v15, 0
	v_pk_mul_f16 v75, v59, v75
	v_exp_f32_e32 v112, v112
	v_exp_f32_e32 v113, v113
	v_mfma_f32_16x16x32_f16 v[76:79], v[72:75], v[24:27], v[76:79]
	ds_read_b128 v[52:55], v2 offset:49152
	v_exp_f32_e32 v114, v114
	v_exp_f32_e32 v115, v115
	s_waitcnt lgkmcnt(1)
	v_mfma_f32_32x32x16_f16 v[96:111], v[32:35], v[28:31], 0
	ds_read_u16 v32, v10 offset:32
	ds_read_b128 v[56:59], v2 offset:50176
	v_fmac_f32_e32 v144, v112, v175
	v_exp_f32_e32 v116, v116
	v_fmac_f32_e32 v145, v113, v144
	v_exp_f32_e32 v117, v117
	v_fmac_f32_e32 v146, v114, v145
	v_cvt_pkrtz_f16_f32 v68, v144, v145
	v_exp_f32_e32 v118, v118
	v_fmac_f32_e32 v147, v115, v146
	v_pk_mul_f16 v68, v60, v68
	v_exp_f32_e32 v119, v119
	v_mfma_f32_32x32x16_f16 v[128:143], v[36:39], v[44:47], 0
	ds_read_b128 v[44:47], v2 offset:18432
	v_fmac_f32_e32 v148, v116, v147
	v_cvt_pkrtz_f16_f32 v69, v146, v147
	v_exp_f32_e32 v120, v120
	v_fmac_f32_e32 v149, v117, v148
	v_pk_mul_f16 v69, v61, v69
	v_exp_f32_e32 v121, v121
	v_fmac_f32_e32 v150, v118, v149
	v_cvt_pkrtz_f16_f32 v70, v148, v149
	v_exp_f32_e32 v122, v122
	v_fmac_f32_e32 v151, v119, v150
	v_pk_mul_f16 v70, v62, v70
	v_exp_f32_e32 v123, v123
	v_mfma_f32_32x32x16_f16 v[160:175], v[36:39], v[48:51], 0
	ds_read_b128 v[36:39], v13 offset:256
	ds_read_b128 v[48:51], v2 offset:19456
	v_cvt_pkrtz_f16_f32 v71, v150, v151
	v_fmac_f32_e32 v184, v120, v151
	v_pk_mul_f16 v71, v63, v71
	v_exp_f32_e32 v124, v124
	v_fmac_f32_e32 v185, v121, v184
	v_mfma_f32_16x16x32_f16 v[80:83], v[68:71], v[20:23], 0
	v_cvt_pkrtz_f16_f32 v72, v184, v185
	v_exp_f32_e32 v125, v125
	v_fmac_f32_e32 v186, v122, v185
	v_pk_mul_f16 v72, v64, v72
	v_add_f32_e32 v84, v76, v77
	v_fmac_f32_e32 v187, v123, v186
	v_exp_f32_e32 v126, v126
	v_cvt_pkrtz_f16_f32 v73, v186, v187
	v_fmac_f32_e32 v188, v124, v187
	v_pk_mul_f16 v73, v65, v73
	v_add_f32_e32 v85, v78, v79
	v_fmac_f32_e32 v189, v125, v188
	v_exp_f32_e32 v127, v127
	v_cvt_pkrtz_f16_f32 v74, v188, v189
	v_fmac_f32_e32 v190, v126, v189
	v_add_f32_e32 v84, v84, v85
	v_fmac_f32_e32 v191, v127, v190
	v_pk_mul_f16 v74, v66, v74
	v_cvt_pkrtz_f16_f32 v75, v190, v191
	v_mfma_f32_16x16x4_f32 a[24:27], v84, v15, 0
	v_pk_mul_f16 v75, v67, v75
	v_exp_f32_e32 v96, v96
	v_exp_f32_e32 v97, v97
	v_mfma_f32_16x16x32_f16 v[80:83], v[72:75], v[24:27], v[80:83]
	ds_read_b128 v[60:63], v2 offset:51200
	v_exp_f32_e32 v98, v98
	v_exp_f32_e32 v99, v99
	s_waitcnt lgkmcnt(1)
	v_mfma_f32_32x32x16_f16 v[112:127], v[32:35], v[28:31], 0
	ds_read_u16 v32, v10 offset:64
	ds_read_b128 v[64:67], v2 offset:52224
	v_fmac_f32_e32 v128, v96, v191
	v_exp_f32_e32 v100, v100
	v_fmac_f32_e32 v129, v97, v128
	v_exp_f32_e32 v101, v101
	v_fmac_f32_e32 v130, v98, v129
	v_cvt_pkrtz_f16_f32 v68, v128, v129
	v_exp_f32_e32 v102, v102
	v_fmac_f32_e32 v131, v99, v130
	v_pk_mul_f16 v68, v52, v68
	v_exp_f32_e32 v103, v103
	v_mfma_f32_32x32x16_f16 v[144:159], v[36:39], v[44:47], 0
	ds_read_b128 v[44:47], v2 offset:20480
	v_fmac_f32_e32 v132, v100, v131
	v_cvt_pkrtz_f16_f32 v69, v130, v131
	v_exp_f32_e32 v104, v104
	v_fmac_f32_e32 v133, v101, v132
	v_pk_mul_f16 v69, v53, v69
	v_exp_f32_e32 v105, v105
	v_fmac_f32_e32 v134, v102, v133
	v_cvt_pkrtz_f16_f32 v70, v132, v133
	v_exp_f32_e32 v106, v106
	v_fmac_f32_e32 v135, v103, v134
	v_pk_mul_f16 v70, v54, v70
	v_exp_f32_e32 v107, v107
	v_mfma_f32_32x32x16_f16 v[176:191], v[36:39], v[48:51], 0
	ds_read_b128 v[36:39], v13 offset:512
	ds_read_b128 v[48:51], v2 offset:21504
	v_cvt_pkrtz_f16_f32 v71, v134, v135
	v_fmac_f32_e32 v168, v104, v135
	v_pk_mul_f16 v71, v55, v71
	v_exp_f32_e32 v108, v108
	v_fmac_f32_e32 v169, v105, v168
	v_mfma_f32_16x16x32_f16 v[76:79], v[68:71], v[20:23], 0
	v_cvt_pkrtz_f16_f32 v72, v168, v169
	v_exp_f32_e32 v109, v109
	v_fmac_f32_e32 v170, v106, v169
	v_pk_mul_f16 v72, v56, v72
	v_add_f32_e32 v84, v80, v81
	v_fmac_f32_e32 v171, v107, v170
	v_exp_f32_e32 v110, v110
	v_cvt_pkrtz_f16_f32 v73, v170, v171
	v_fmac_f32_e32 v172, v108, v171
	v_pk_mul_f16 v73, v57, v73
	v_add_f32_e32 v85, v82, v83
	v_fmac_f32_e32 v173, v109, v172
	v_exp_f32_e32 v111, v111
	v_cvt_pkrtz_f16_f32 v74, v172, v173
	v_fmac_f32_e32 v174, v110, v173
	v_add_f32_e32 v84, v84, v85
	v_fmac_f32_e32 v175, v111, v174
	v_pk_mul_f16 v74, v58, v74
	v_cvt_pkrtz_f16_f32 v75, v174, v175
	v_mfma_f32_16x16x4_f32 a[28:31], v84, v15, 0
	v_pk_mul_f16 v75, v59, v75
	v_exp_f32_e32 v112, v112
	v_exp_f32_e32 v113, v113
	v_mfma_f32_16x16x32_f16 v[76:79], v[72:75], v[24:27], v[76:79]
	ds_read_b128 v[52:55], v2 offset:53248
	v_exp_f32_e32 v114, v114
	v_exp_f32_e32 v115, v115
	s_waitcnt lgkmcnt(1)
	v_mfma_f32_32x32x16_f16 v[96:111], v[32:35], v[28:31], 0
	ds_read_u16 v32, v10 offset:96
	ds_read_b128 v[56:59], v2 offset:54272
	v_fmac_f32_e32 v144, v112, v175
	v_exp_f32_e32 v116, v116
	v_fmac_f32_e32 v145, v113, v144
	v_exp_f32_e32 v117, v117
	v_fmac_f32_e32 v146, v114, v145
	v_cvt_pkrtz_f16_f32 v68, v144, v145
	v_exp_f32_e32 v118, v118
	v_fmac_f32_e32 v147, v115, v146
	v_pk_mul_f16 v68, v60, v68
	v_exp_f32_e32 v119, v119
	v_mfma_f32_32x32x16_f16 v[128:143], v[36:39], v[44:47], 0
	ds_read_b128 v[44:47], v2 offset:22528
	v_fmac_f32_e32 v148, v116, v147
	v_cvt_pkrtz_f16_f32 v69, v146, v147
	v_exp_f32_e32 v120, v120
	v_fmac_f32_e32 v149, v117, v148
	v_pk_mul_f16 v69, v61, v69
	v_exp_f32_e32 v121, v121
	v_fmac_f32_e32 v150, v118, v149
	v_cvt_pkrtz_f16_f32 v70, v148, v149
	v_exp_f32_e32 v122, v122
	v_fmac_f32_e32 v151, v119, v150
	v_pk_mul_f16 v70, v62, v70
	v_exp_f32_e32 v123, v123
	v_mfma_f32_32x32x16_f16 v[160:175], v[36:39], v[48:51], 0
	ds_read_b128 v[36:39], v13 offset:768
	ds_read_b128 v[48:51], v2 offset:23552
	v_cvt_pkrtz_f16_f32 v71, v150, v151
	v_fmac_f32_e32 v184, v120, v151
	v_pk_mul_f16 v71, v63, v71
	v_exp_f32_e32 v124, v124
	v_fmac_f32_e32 v185, v121, v184
	v_mfma_f32_16x16x32_f16 v[80:83], v[68:71], v[20:23], 0
	v_cvt_pkrtz_f16_f32 v72, v184, v185
	v_exp_f32_e32 v125, v125
	v_fmac_f32_e32 v186, v122, v185
	v_pk_mul_f16 v72, v64, v72
	v_add_f32_e32 v84, v76, v77
	v_fmac_f32_e32 v187, v123, v186
	v_exp_f32_e32 v126, v126
	v_cvt_pkrtz_f16_f32 v73, v186, v187
	v_fmac_f32_e32 v188, v124, v187
	v_pk_mul_f16 v73, v65, v73
	v_add_f32_e32 v85, v78, v79
	v_fmac_f32_e32 v189, v125, v188
	v_exp_f32_e32 v127, v127
	v_cvt_pkrtz_f16_f32 v74, v188, v189
	v_fmac_f32_e32 v190, v126, v189
	v_add_f32_e32 v84, v84, v85
	v_fmac_f32_e32 v191, v127, v190
	v_pk_mul_f16 v74, v66, v74
	v_cvt_pkrtz_f16_f32 v75, v190, v191
	v_mfma_f32_16x16x4_f32 a[0:3], v84, v15, 0
	v_pk_mul_f16 v75, v67, v75
	v_exp_f32_e32 v96, v96
	v_exp_f32_e32 v97, v97
	v_mfma_f32_16x16x32_f16 v[80:83], v[72:75], v[24:27], v[80:83]
	ds_read_b128 v[60:63], v2 offset:55296
	v_exp_f32_e32 v98, v98
	v_exp_f32_e32 v99, v99
	s_waitcnt lgkmcnt(1)
	v_mfma_f32_32x32x16_f16 v[112:127], v[32:35], v[28:31], 0
	ds_read_u16 v32, v10 offset:128
	ds_read_b128 v[64:67], v2 offset:56320
	v_fmac_f32_e32 v128, v96, v191
	v_exp_f32_e32 v100, v100
	v_fmac_f32_e32 v129, v97, v128
	v_exp_f32_e32 v101, v101
	v_fmac_f32_e32 v130, v98, v129
	v_cvt_pkrtz_f16_f32 v68, v128, v129
	v_exp_f32_e32 v102, v102
	v_fmac_f32_e32 v131, v99, v130
	v_pk_mul_f16 v68, v52, v68
	v_exp_f32_e32 v103, v103
	v_mfma_f32_32x32x16_f16 v[144:159], v[36:39], v[44:47], 0
	ds_read_b128 v[44:47], v2 offset:24576
	v_fmac_f32_e32 v132, v100, v131
	v_cvt_pkrtz_f16_f32 v69, v130, v131
	v_exp_f32_e32 v104, v104
	v_fmac_f32_e32 v133, v101, v132
	v_pk_mul_f16 v69, v53, v69
	v_exp_f32_e32 v105, v105
	v_fmac_f32_e32 v134, v102, v133
	v_cvt_pkrtz_f16_f32 v70, v132, v133
	v_exp_f32_e32 v106, v106
	v_fmac_f32_e32 v135, v103, v134
	v_pk_mul_f16 v70, v54, v70
	v_exp_f32_e32 v107, v107
	v_mfma_f32_32x32x16_f16 v[176:191], v[36:39], v[48:51], 0
	ds_read_b128 v[36:39], v13 offset:1024
	ds_read_b128 v[48:51], v2 offset:25600
	v_cvt_pkrtz_f16_f32 v71, v134, v135
	v_fmac_f32_e32 v168, v104, v135
	v_pk_mul_f16 v71, v55, v71
	v_exp_f32_e32 v108, v108
	v_fmac_f32_e32 v169, v105, v168
	v_mfma_f32_16x16x32_f16 v[76:79], v[68:71], v[20:23], 0
	v_cvt_pkrtz_f16_f32 v72, v168, v169
	v_exp_f32_e32 v109, v109
	v_fmac_f32_e32 v170, v106, v169
	v_pk_mul_f16 v72, v56, v72
	v_add_f32_e32 v84, v80, v81
	v_fmac_f32_e32 v171, v107, v170
	v_exp_f32_e32 v110, v110
	v_cvt_pkrtz_f16_f32 v73, v170, v171
	v_fmac_f32_e32 v172, v108, v171
	v_pk_mul_f16 v73, v57, v73
	v_add_f32_e32 v85, v82, v83
	v_fmac_f32_e32 v173, v109, v172
	v_exp_f32_e32 v111, v111
	v_cvt_pkrtz_f16_f32 v74, v172, v173
	v_fmac_f32_e32 v174, v110, v173
	v_add_f32_e32 v84, v84, v85
	v_fmac_f32_e32 v175, v111, v174
	v_pk_mul_f16 v74, v58, v74
	v_cvt_pkrtz_f16_f32 v75, v174, v175
	v_mfma_f32_16x16x4_f32 a[4:7], v84, v15, 0
	v_pk_mul_f16 v75, v59, v75
	v_exp_f32_e32 v112, v112
	v_exp_f32_e32 v113, v113
	v_mfma_f32_16x16x32_f16 v[76:79], v[72:75], v[24:27], v[76:79]
	ds_read_b128 v[52:55], v2 offset:57344
	v_exp_f32_e32 v114, v114
	v_exp_f32_e32 v115, v115
	s_waitcnt lgkmcnt(1)
	v_mfma_f32_32x32x16_f16 v[96:111], v[32:35], v[28:31], 0
	ds_read_u16 v32, v10 offset:160
	ds_read_b128 v[56:59], v2 offset:58368
	v_fmac_f32_e32 v144, v112, v175
	v_exp_f32_e32 v116, v116
	v_fmac_f32_e32 v145, v113, v144
	v_exp_f32_e32 v117, v117
	v_fmac_f32_e32 v146, v114, v145
	v_cvt_pkrtz_f16_f32 v68, v144, v145
	v_exp_f32_e32 v118, v118
	v_fmac_f32_e32 v147, v115, v146
	v_pk_mul_f16 v68, v60, v68
	v_exp_f32_e32 v119, v119
	v_mfma_f32_32x32x16_f16 v[128:143], v[36:39], v[44:47], 0
	ds_read_b128 v[44:47], v2 offset:26624
	v_fmac_f32_e32 v148, v116, v147
	v_cvt_pkrtz_f16_f32 v69, v146, v147
	v_exp_f32_e32 v120, v120
	v_fmac_f32_e32 v149, v117, v148
	v_pk_mul_f16 v69, v61, v69
	v_exp_f32_e32 v121, v121
	v_fmac_f32_e32 v150, v118, v149
	v_cvt_pkrtz_f16_f32 v70, v148, v149
	v_exp_f32_e32 v122, v122
	v_fmac_f32_e32 v151, v119, v150
	v_pk_mul_f16 v70, v62, v70
	v_exp_f32_e32 v123, v123
	v_mfma_f32_32x32x16_f16 v[160:175], v[36:39], v[48:51], 0
	ds_read_b128 v[36:39], v13 offset:1280
	ds_read_b128 v[48:51], v2 offset:27648
	v_cvt_pkrtz_f16_f32 v71, v150, v151
	v_fmac_f32_e32 v184, v120, v151
	v_pk_mul_f16 v71, v63, v71
	v_exp_f32_e32 v124, v124
	v_fmac_f32_e32 v185, v121, v184
	v_mfma_f32_16x16x32_f16 v[80:83], v[68:71], v[20:23], 0
	v_cvt_pkrtz_f16_f32 v72, v184, v185
	v_exp_f32_e32 v125, v125
	v_fmac_f32_e32 v186, v122, v185
	v_pk_mul_f16 v72, v64, v72
	v_add_f32_e32 v84, v76, v77
	v_fmac_f32_e32 v187, v123, v186
	v_exp_f32_e32 v126, v126
	v_cvt_pkrtz_f16_f32 v73, v186, v187
	v_fmac_f32_e32 v188, v124, v187
	v_pk_mul_f16 v73, v65, v73
	v_add_f32_e32 v85, v78, v79
	v_fmac_f32_e32 v189, v125, v188
	v_exp_f32_e32 v127, v127
	v_cvt_pkrtz_f16_f32 v74, v188, v189
	v_fmac_f32_e32 v190, v126, v189
	v_add_f32_e32 v84, v84, v85
	v_fmac_f32_e32 v191, v127, v190
	v_pk_mul_f16 v74, v66, v74
	v_cvt_pkrtz_f16_f32 v75, v190, v191
	v_mfma_f32_16x16x4_f32 a[8:11], v84, v15, 0
	v_pk_mul_f16 v75, v67, v75
	v_exp_f32_e32 v96, v96
	v_exp_f32_e32 v97, v97
	v_mfma_f32_16x16x32_f16 v[80:83], v[72:75], v[24:27], v[80:83]
	ds_read_b128 v[60:63], v2 offset:59392
	v_exp_f32_e32 v98, v98
	v_exp_f32_e32 v99, v99
	s_waitcnt lgkmcnt(1)
	v_mfma_f32_32x32x16_f16 v[112:127], v[32:35], v[28:31], 0
	ds_read_u16 v32, v10 offset:192
	ds_read_b128 v[64:67], v2 offset:60416
	v_fmac_f32_e32 v128, v96, v191
	v_exp_f32_e32 v100, v100
	v_fmac_f32_e32 v129, v97, v128
	v_exp_f32_e32 v101, v101
	v_fmac_f32_e32 v130, v98, v129
	v_cvt_pkrtz_f16_f32 v68, v128, v129
	v_exp_f32_e32 v102, v102
	v_fmac_f32_e32 v131, v99, v130
	v_pk_mul_f16 v68, v52, v68
	v_exp_f32_e32 v103, v103
	v_mfma_f32_32x32x16_f16 v[144:159], v[36:39], v[44:47], 0
	ds_read_b128 v[44:47], v2 offset:28672
	v_fmac_f32_e32 v132, v100, v131
	v_cvt_pkrtz_f16_f32 v69, v130, v131
	v_exp_f32_e32 v104, v104
	v_fmac_f32_e32 v133, v101, v132
	v_pk_mul_f16 v69, v53, v69
	v_exp_f32_e32 v105, v105
	v_fmac_f32_e32 v134, v102, v133
	v_cvt_pkrtz_f16_f32 v70, v132, v133
	v_exp_f32_e32 v106, v106
	v_fmac_f32_e32 v135, v103, v134
	v_pk_mul_f16 v70, v54, v70
	v_exp_f32_e32 v107, v107
	v_mfma_f32_32x32x16_f16 v[176:191], v[36:39], v[48:51], 0
	ds_read_b128 v[36:39], v13 offset:1536
	ds_read_b128 v[48:51], v2 offset:29696
	v_cvt_pkrtz_f16_f32 v71, v134, v135
	v_fmac_f32_e32 v168, v104, v135
	v_pk_mul_f16 v71, v55, v71
	v_exp_f32_e32 v108, v108
	v_fmac_f32_e32 v169, v105, v168
	v_mfma_f32_16x16x32_f16 v[76:79], v[68:71], v[20:23], 0
	v_cvt_pkrtz_f16_f32 v72, v168, v169
	v_exp_f32_e32 v109, v109
	v_fmac_f32_e32 v170, v106, v169
	v_pk_mul_f16 v72, v56, v72
	v_add_f32_e32 v84, v80, v81
	v_fmac_f32_e32 v171, v107, v170
	v_exp_f32_e32 v110, v110
	v_cvt_pkrtz_f16_f32 v73, v170, v171
	v_fmac_f32_e32 v172, v108, v171
	v_pk_mul_f16 v73, v57, v73
	v_add_f32_e32 v85, v82, v83
	v_fmac_f32_e32 v173, v109, v172
	v_exp_f32_e32 v111, v111
	v_cvt_pkrtz_f16_f32 v74, v172, v173
	v_fmac_f32_e32 v174, v110, v173
	v_add_f32_e32 v84, v84, v85
	v_fmac_f32_e32 v175, v111, v174
	v_pk_mul_f16 v74, v58, v74
	v_cvt_pkrtz_f16_f32 v75, v174, v175
	v_mfma_f32_16x16x4_f32 a[12:15], v84, v15, 0
	v_pk_mul_f16 v75, v59, v75
	v_exp_f32_e32 v112, v112
	v_exp_f32_e32 v113, v113
	v_mfma_f32_16x16x32_f16 v[76:79], v[72:75], v[24:27], v[76:79]
	ds_read_b128 v[52:55], v2 offset:61440
	v_exp_f32_e32 v114, v114
	v_exp_f32_e32 v115, v115
	s_waitcnt lgkmcnt(1)
	v_mfma_f32_32x32x16_f16 v[96:111], v[32:35], v[28:31], 0
	ds_read_u16 v32, v10 offset:224
	ds_read_b128 v[56:59], v2 offset:62464
	v_fmac_f32_e32 v144, v112, v175
	v_exp_f32_e32 v116, v116
	v_fmac_f32_e32 v145, v113, v144
	v_exp_f32_e32 v117, v117
	v_fmac_f32_e32 v146, v114, v145
	v_cvt_pkrtz_f16_f32 v68, v144, v145
	v_exp_f32_e32 v118, v118
	v_fmac_f32_e32 v147, v115, v146
	v_pk_mul_f16 v68, v60, v68
	v_exp_f32_e32 v119, v119
	v_mfma_f32_32x32x16_f16 v[128:143], v[36:39], v[44:47], 0
	ds_read_b128 v[44:47], v2 offset:30720
	v_fmac_f32_e32 v148, v116, v147
	v_cvt_pkrtz_f16_f32 v69, v146, v147
	v_exp_f32_e32 v120, v120
	v_fmac_f32_e32 v149, v117, v148
	v_pk_mul_f16 v69, v61, v69
	v_exp_f32_e32 v121, v121
	v_fmac_f32_e32 v150, v118, v149
	v_cvt_pkrtz_f16_f32 v70, v148, v149
	v_exp_f32_e32 v122, v122
	v_fmac_f32_e32 v151, v119, v150
	v_pk_mul_f16 v70, v62, v70
	v_exp_f32_e32 v123, v123
	v_mfma_f32_32x32x16_f16 v[160:175], v[36:39], v[48:51], 0
	ds_read_b128 v[36:39], v13 offset:1792
	ds_read_b128 v[48:51], v2 offset:31744
	v_cvt_pkrtz_f16_f32 v71, v150, v151
	v_fmac_f32_e32 v184, v120, v151
	v_pk_mul_f16 v71, v63, v71
	v_exp_f32_e32 v124, v124
	v_fmac_f32_e32 v185, v121, v184
	v_mfma_f32_16x16x32_f16 v[80:83], v[68:71], v[20:23], 0
	v_cvt_pkrtz_f16_f32 v72, v184, v185
	v_exp_f32_e32 v125, v125
	v_fmac_f32_e32 v186, v122, v185
	v_pk_mul_f16 v72, v64, v72
	v_add_f32_e32 v84, v76, v77
	v_fmac_f32_e32 v187, v123, v186
	v_exp_f32_e32 v126, v126
	v_cvt_pkrtz_f16_f32 v73, v186, v187
	v_fmac_f32_e32 v188, v124, v187
	v_pk_mul_f16 v73, v65, v73
	v_add_f32_e32 v85, v78, v79
	v_fmac_f32_e32 v189, v125, v188
	v_exp_f32_e32 v127, v127
	v_cvt_pkrtz_f16_f32 v74, v188, v189
	v_fmac_f32_e32 v190, v126, v189
	v_add_f32_e32 v84, v84, v85
	v_fmac_f32_e32 v191, v127, v190
	v_pk_mul_f16 v74, v66, v74
	v_cvt_pkrtz_f16_f32 v75, v190, v191
	v_mfma_f32_16x16x4_f32 a[16:19], v84, v15, 0
	v_pk_mul_f16 v75, v67, v75
	v_exp_f32_e32 v96, v96
	v_exp_f32_e32 v97, v97
	v_mfma_f32_16x16x32_f16 v[80:83], v[72:75], v[24:27], v[80:83]
	ds_read_b128 v[60:63], v2 offset:63488
	ds_read_b128 v[64:67], v2 offset:64512
	s_waitcnt vmcnt(0)
	ds_write_b16 v8, v18 offset:512
	ds_write_b16 v8, v19 offset:1536
	s_waitcnt lgkmcnt(0)
	s_barrier
	s_cmp_ge_u32 s40, 15
	s_cbranch_scc1 .Lscan_nodma1
	s_add_i32 m0, s32, 0x4000
	s_nop 0
	global_load_lds_dwordx4 v2, s[20:21]
	s_add_i32 m0, s32, 49152
	s_nop 0
	global_load_lds_dwordx4 v2, s[22:23]
	s_add_i32 m0, s33, 0x4000
	s_nop 0
	global_load_lds_dwordx4 v3, s[20:21]
	s_add_i32 m0, s33, 49152
	s_nop 0
	global_load_lds_dwordx4 v3, s[22:23]
	s_add_i32 m0, s34, 0x4000
	s_nop 0
	global_load_lds_dwordx4 v4, s[20:21]
	s_add_i32 m0, s34, 49152
	s_nop 0
	global_load_lds_dwordx4 v4, s[22:23]
	s_add_i32 m0, s35, 0x4000
	s_nop 0
	global_load_lds_dwordx4 v5, s[20:21]
	s_add_i32 m0, s35, 49152
	s_nop 0
	global_load_lds_dwordx4 v5, s[22:23]
	s_add_i32 m0, s28, 0x100
	s_nop 0
	global_load_lds_dword v6, s[24:25]
	global_load_ushort v18, v7, s[26:27]
	global_load_ushort v19, v7, s[26:27] offset:128
	s_add_u32 s20, s20, 0x4000
	s_addc_u32 s21, s21, 0
	s_add_u32 s22, s22, 0x4000
	s_addc_u32 s23, s23, 0
	s_add_u32 s24, s24, 0x100
	s_addc_u32 s25, s25, 0
	s_add_u32 s26, s26, 0x100
	s_addc_u32 s27, s27, 0
.Lscan_nodma1:
	s_and_saveexec_b64 s[44:45], s[42:43]
	global_store_dwordx4 v[16:17], a[20:23], off offset:-192
	global_store_dwordx4 v[16:17], a[24:27], off offset:-128
	global_store_dwordx4 v[16:17], a[28:31], off offset:-64
	global_store_dwordx4 v[16:17], a[0:3], off
	global_store_dwordx4 v[16:17], a[4:7], off offset:64
	global_store_dwordx4 v[16:17], a[8:11], off offset:128
	global_store_dwordx4 v[16:17], a[12:15], off offset:192
	global_store_dwordx4 v[16:17], a[16:19], off offset:256
	s_mov_b64 exec, s[44:45]
	v_lshl_add_u64 v[16:17], v[16:17], 0, s[46:47]
	v_exp_f32_e32 v98, v98
	v_exp_f32_e32 v99, v99
	s_waitcnt lgkmcnt(1)
	v_mfma_f32_32x32x16_f16 v[112:127], v[32:35], v[28:31], 0
	ds_read_u16 v32, v9 offset:0
	v_fmac_f32_e32 v128, v96, v191
	v_exp_f32_e32 v100, v100
	v_fmac_f32_e32 v129, v97, v128
	v_exp_f32_e32 v101, v101
	v_fmac_f32_e32 v130, v98, v129
	v_cvt_pkrtz_f16_f32 v68, v128, v129
	v_exp_f32_e32 v102, v102
	v_fmac_f32_e32 v131, v99, v130
	v_pk_mul_f16 v68, v52, v68
	v_exp_f32_e32 v103, v103
	v_mfma_f32_32x32x16_f16 v[144:159], v[36:39], v[44:47], 0
	ds_read_b128 v[44:47], v2 offset:0
	v_fmac_f32_e32 v132, v100, v131
	v_cvt_pkrtz_f16_f32 v69, v130, v131
	v_exp_f32_e32 v104, v104
	v_fmac_f32_e32 v133, v101, v132
	v_pk_mul_f16 v69, v53, v69
	v_exp_f32_e32 v105, v105
	v_fmac_f32_e32 v134, v102, v133
	v_cvt_pkrtz_f16_f32 v70, v132, v133
	v_exp_f32_e32 v106, v106
	v_fmac_f32_e32 v135, v103, v134
	v_pk_mul_f16 v70, v54, v70
	v_exp_f32_e32 v107, v107
	v_mfma_f32_32x32x16_f16 v[176:191], v[36:39], v[48:51], 0
	ds_read_b128 v[36:39], v11 offset:0
	ds_read_b128 v[48:51], v2 offset:1024
	v_cvt_pkrtz_f16_f32 v71, v134, v135
	v_fmac_f32_e32 v168, v104, v135
	v_pk_mul_f16 v71, v55, v71
	v_exp_f32_e32 v108, v108
	v_fmac_f32_e32 v169, v105, v168
	v_mfma_f32_16x16x32_f16 v[76:79], v[68:71], v[20:23], 0
	v_cvt_pkrtz_f16_f32 v72, v168, v169
	v_exp_f32_e32 v109, v109
	v_fmac_f32_e32 v170, v106, v169
	v_pk_mul_f16 v72, v56, v72
	v_add_f32_e32 v84, v80, v81
	v_fmac_f32_e32 v171, v107, v170
	v_exp_f32_e32 v110, v110
	v_cvt_pkrtz_f16_f32 v73, v170, v171
	v_fmac_f32_e32 v172, v108, v171
	v_pk_mul_f16 v73, v57, v73
	v_add_f32_e32 v85, v82, v83
	v_fmac_f32_e32 v173, v109, v172
	v_exp_f32_e32 v111, v111
	v_cvt_pkrtz_f16_f32 v74, v172, v173
	v_fmac_f32_e32 v174, v110, v173
	v_add_f32_e32 v84, v84, v85
	v_fmac_f32_e32 v175, v111, v174
	v_pk_mul_f16 v74, v58, v74
	v_cvt_pkrtz_f16_f32 v75, v174, v175
	v_mfma_f32_16x16x4_f32 a[20:23], v84, v15, 0
	v_pk_mul_f16 v75, v59, v75
	v_exp_f32_e32 v112, v112
	v_exp_f32_e32 v113, v113
	v_mfma_f32_16x16x32_f16 v[76:79], v[72:75], v[24:27], v[76:79]
	ds_read_b128 v[52:55], v2 offset:32768
	v_exp_f32_e32 v114, v114
	v_exp_f32_e32 v115, v115
	s_waitcnt lgkmcnt(1)
	v_mfma_f32_32x32x16_f16 v[96:111], v[32:35], v[28:31], 0
	ds_read_u16 v32, v9 offset:32
	ds_read_b128 v[56:59], v2 offset:33792
	v_fmac_f32_e32 v144, v112, v175
	v_exp_f32_e32 v116, v116
	v_fmac_f32_e32 v145, v113, v144
	v_exp_f32_e32 v117, v117
	v_fmac_f32_e32 v146, v114, v145
	v_cvt_pkrtz_f16_f32 v68, v144, v145
	v_exp_f32_e32 v118, v118
	v_fmac_f32_e32 v147, v115, v146
	v_pk_mul_f16 v68, v60, v68
	v_exp_f32_e32 v119, v119
	v_mfma_f32_32x32x16_f16 v[128:143], v[36:39], v[44:47], 0
	ds_read_b128 v[44:47], v2 offset:2048
	v_fmac_f32_e32 v148, v116, v147
	v_cvt_pkrtz_f16_f32 v69, v146, v147
	v_exp_f32_e32 v120, v120
	v_fmac_f32_e32 v149, v117, v148
	v_pk_mul_f16 v69, v61, v69
	v_exp_f32_e32 v121, v121
	v_fmac_f32_e32 v150, v118, v149
	v_cvt_pkrtz_f16_f32 v70, v148, v149
	v_exp_f32_e32 v122, v122
	v_fmac_f32_e32 v151, v119, v150
	v_pk_mul_f16 v70, v62, v70
	v_exp_f32_e32 v123, v123
	v_mfma_f32_32x32x16_f16 v[160:175], v[36:39], v[48:51], 0
	ds_read_b128 v[36:39], v11 offset:256
	ds_read_b128 v[48:51], v2 offset:3072
	v_cvt_pkrtz_f16_f32 v71, v150, v151
	v_fmac_f32_e32 v184, v120, v151
	v_pk_mul_f16 v71, v63, v71
	v_exp_f32_e32 v124, v124
	v_fmac_f32_e32 v185, v121, v184
	v_mfma_f32_16x16x32_f16 v[80:83], v[68:71], v[20:23], 0
	v_cvt_pkrtz_f16_f32 v72, v184, v185
	v_exp_f32_e32 v125, v125
	v_fmac_f32_e32 v186, v122, v185
	v_pk_mul_f16 v72, v64, v72
	v_add_f32_e32 v84, v76, v77
	v_fmac_f32_e32 v187, v123, v186
	v_exp_f32_e32 v126, v126
	v_cvt_pkrtz_f16_f32 v73, v186, v187
	v_fmac_f32_e32 v188, v124, v187
	v_pk_mul_f16 v73, v65, v73
	v_add_f32_e32 v85, v78, v79
	v_fmac_f32_e32 v189, v125, v188
	v_exp_f32_e32 v127, v127
	v_cvt_pkrtz_f16_f32 v74, v188, v189
	v_fmac_f32_e32 v190, v126, v189
	v_add_f32_e32 v84, v84, v85
	v_fmac_f32_e32 v191, v127, v190
	v_pk_mul_f16 v74, v66, v74
	v_cvt_pkrtz_f16_f32 v75, v190, v191
	v_mfma_f32_16x16x4_f32 a[24:27], v84, v15, 0
	v_pk_mul_f16 v75, v67, v75
	s_add_u32 s40, s40, 1
	s_cmp_lt_u32 s40, 16
	s_cbranch_scc1 .Lscan_loop
	s_nop 1
	v_mfma_f32_16x16x32_f16 v[80:83], v[72:75], v[24:27], v[80:83]
	s_nop 15
	v_add_f32_e32 v84, v80, v81
	v_add_f32_e32 v85, v82, v83
	s_nop 0
	v_add_f32_e32 v84, v84, v85
	s_nop 1
	v_mfma_f32_16x16x4_f32 a[28:31], v84, v15, 0
	s_nop 15
	s_nop 3
	s_and_saveexec_b64 s[44:45], s[42:43]
	global_store_dwordx4 v[16:17], a[20:23], off offset:-192
	global_store_dwordx4 v[16:17], a[24:27], off offset:-128
	global_store_dwordx4 v[16:17], a[28:31], off offset:-64
	s_endpgm

	.amdhsa_kernel _Z6scan_kPKDF16_S0_S0_S0_PKfPf
		.amdhsa_group_segment_fixed_size 86016
		.amdhsa_private_segment_fixed_size 0
		.amdhsa_kernarg_size 48
		.amdhsa_user_sgpr_count 2
		.amdhsa_user_sgpr_dispatch_ptr 0
		.amdhsa_user_sgpr_queue_ptr 0
		.amdhsa_user_sgpr_kernarg_segment_ptr 1
		.amdhsa_user_sgpr_dispatch_id 0
		.amdhsa_user_sgpr_kernarg_preload_length 0
		.amdhsa_user_sgpr_kernarg_preload_offset 0
		.amdhsa_user_sgpr_private_segment_size 0
		.amdhsa_uses_dynamic_stack 0
		.amdhsa_enable_private_segment 0
		.amdhsa_system_sgpr_workgroup_id_x 1
		.amdhsa_system_sgpr_workgroup_id_y 0
		.amdhsa_system_sgpr_workgroup_id_z 0
		.amdhsa_system_sgpr_workgroup_info 0
		.amdhsa_system_vgpr_workitem_id 0
		.amdhsa_next_free_vgpr 224
		.amdhsa_next_free_sgpr 96
		.amdhsa_accum_offset 192
		.amdhsa_reserve_vcc 1
		.amdhsa_float_round_mode_32 0
		.amdhsa_float_round_mode_16_64 0
		.amdhsa_float_denorm_mode_32 3
		.amdhsa_float_denorm_mode_16_64 3
		.amdhsa_dx10_clamp 1
		.amdhsa_ieee_mode 1
		.amdhsa_fp16_overflow 0
		.amdhsa_tg_split 0
		.amdhsa_exception_fp_ieee_invalid_op 0
		.amdhsa_exception_fp_denorm_src 0
		.amdhsa_exception_fp_ieee_div_zero 0
		.amdhsa_exception_fp_ieee_overflow 0
		.amdhsa_exception_fp_ieee_underflow 0
		.amdhsa_exception_fp_ieee_inexact 0
		.amdhsa_exception_int_div_zero 0
	.end_amdhsa_kernel

amdhsa.kernels:
  - .agpr_count:     0
    .args:
      - .offset:         0
        .size:           152
        .value_kind:     by_value
    .group_segment_fixed_size: 7168
    .kernarg_segment_align: 8
    .kernarg_segment_size: 152
    .language:       OpenCL C
    .language_version:
      - 2
      - 0
    .max_flat_workgroup_size: 256
    .name:           _Z6prep_k5PrepP
    .private_segment_fixed_size: 0
    .sgpr_count:     62
    .sgpr_spill_count: 0
    .symbol:         _Z6prep_k5PrepP.kd
    .uniform_work_group_size: 1
    .uses_dynamic_stack: false
    .vgpr_count:     58
    .vgpr_spill_count: 0
    .wavefront_size: 64
  - .agpr_count:     0
    .args:
      - .actual_access:  read_only
        .address_space:  global
        .offset:         0
        .size:           8
        .value_kind:     global_buffer
      - .actual_access:  read_only
        .address_space:  global
        .offset:         8
        .size:           8
        .value_kind:     global_buffer
      - .actual_access:  read_only
        .address_space:  global
        .offset:         16
        .size:           8
        .value_kind:     global_buffer
      - .actual_access:  write_only
        .address_space:  global
        .offset:         24
        .size:           8
        .value_kind:     global_buffer
      - .actual_access:  write_only
        .address_space:  global
        .offset:         32
        .size:           8
        .value_kind:     global_buffer
    .group_segment_fixed_size: 9216
    .kernarg_segment_align: 8
    .kernarg_segment_size: 40
    .language:       OpenCL C
    .language_version:
      - 2
      - 0
    .max_flat_workgroup_size: 256
    .name:           _Z8conv1d_kPKDF16_PKfS2_PDF16_S3_
    .private_segment_fixed_size: 0
    .sgpr_count:     22
    .sgpr_spill_count: 0
    .symbol:         _Z8conv1d_kPKDF16_PKfS2_PDF16_S3_.kd
    .uniform_work_group_size: 1
    .uses_dynamic_stack: false
    .vgpr_count:     53
    .vgpr_spill_count: 0
    .wavefront_size: 64
  - .agpr_count:     4
    .args:
      - .actual_access:  read_only
        .address_space:  global
        .offset:         0
        .size:           8
        .value_kind:     global_buffer
      - .actual_access:  read_only
        .address_space:  global
        .offset:         8
        .size:           8
        .value_kind:     global_buffer
      - .actual_access:  read_only
        .address_space:  global
        .offset:         16
        .size:           8
        .value_kind:     global_buffer
      - .actual_access:  read_only
        .address_space:  global
        .offset:         24
        .size:           8
        .value_kind:     global_buffer
      - .actual_access:  write_only
        .address_space:  global
        .offset:         32
        .size:           8
        .value_kind:     global_buffer
      - .actual_access:  write_only
        .address_space:  global
        .offset:         40
        .size:           8
        .value_kind:     global_buffer
    .group_segment_fixed_size: 70656
    .kernarg_segment_align: 8
    .kernarg_segment_size: 48
    .language:       OpenCL C
    .language_version:
      - 2
      - 0
    .max_flat_workgroup_size: 256
    .name:           _Z4dt_kPKfS0_S0_PKDF16_PDF16_S3_
    .private_segment_fixed_size: 0
    .sgpr_count:     25
    .sgpr_spill_count: 0
    .symbol:         _Z4dt_kPKfS0_S0_PKDF16_PDF16_S3_.kd
    .uniform_work_group_size: 1
    .uses_dynamic_stack: false
    .vgpr_count:     72
    .vgpr_spill_count: 0
    .wavefront_size: 64
  - .agpr_count:     32
    .args:
      - .address_space:  global
        .offset:         0
        .size:           8
        .value_kind:     global_buffer
      - .actual_access:  read_only
        .address_space:  global
        .offset:         8
        .size:           8
        .value_kind:     global_buffer
      - .address_space:  global
        .offset:         16
        .size:           8
        .value_kind:     global_buffer
      - .address_space:  global
        .offset:         24
        .size:           8
        .value_kind:     global_buffer
      - .actual_access:  read_only
        .address_space:  global
        .offset:         32
        .size:           8
        .value_kind:     global_buffer
      - .actual_access:  write_only
        .address_space:  global
        .offset:         40
        .size:           8
        .value_kind:     global_buffer
    .group_segment_fixed_size: 86016
    .kernarg_segment_align: 8
    .kernarg_segment_size: 48
    .language:       OpenCL C
    .language_version:
      - 2
      - 0
    .max_flat_workgroup_size: 256
    .name:           _Z6scan_kPKDF16_S0_S0_S0_PKfPf
    .private_segment_fixed_size: 0
    .sgpr_count:     66
    .sgpr_spill_count: 0
    .symbol:         _Z6scan_kPKDF16_S0_S0_S0_PKfPf.kd
    .uniform_work_group_size: 1
    .uses_dynamic_stack: false
    .vgpr_count:     224
    .vgpr_spill_count: 0
    .wavefront_size: 64
  - .agpr_count:     0
    .args:
      - .actual_access:  read_only
        .address_space:  global
        .offset:         0
        .size:           8
        .value_kind:     global_buffer
      - .actual_access:  read_only
        .address_space:  global
        .offset:         8
        .size:           8
        .value_kind:     global_buffer
      - .actual_access:  read_only
        .address_space:  global
        .offset:         16
        .size:           8
        .value_kind:     global_buffer
      - .actual_access:  read_only
        .address_space:  global
        .offset:         24
        .size:           8
        .value_kind:     global_buffer
      - .actual_access:  write_only
        .address_space:  global
        .offset:         32
        .size:           8
        .value_kind:     global_buffer
    .group_segment_fixed_size: 9216
    .kernarg_segment_align: 8
    .kernarg_segment_size: 40
    .language:       OpenCL C
    .language_version:
      - 2
      - 0
    .max_flat_workgroup_size: 256
    .name:           _Z6gate_kPKfPKDF16_S2_S0_PDF16_
    .private_segment_fixed_size: 0
    .sgpr_count:     22
    .sgpr_spill_count: 0
    .symbol:         _Z6gate_kPKfPKDF16_S2_S0_PDF16_.kd
    .uniform_work_group_size: 1
    .uses_dynamic_stack: false
    .vgpr_count:     46
    .vgpr_spill_count: 0
    .wavefront_size: 64
  - .agpr_count:     0
    .args:
      - .actual_access:  read_only
        .address_space:  global
        .offset:         0
        .size:           8
        .value_kind:     global_buffer
      - .actual_access:  read_only
        .address_space:  global
        .offset:         8
        .size:           8
        .value_kind:     global_buffer
      - .actual_access:  read_only
        .address_space:  global
        .offset:         16
        .size:           8
        .value_kind:     global_buffer
      - .actual_access:  write_only
        .address_space:  global
        .offset:         24
        .size:           8
        .value_kind:     global_buffer
    .group_segment_fixed_size: 6912
    .kernarg_segment_align: 8
    .kernarg_segment_size: 32
    .language:       OpenCL C
    .language_version:
      - 2
      - 0
    .max_flat_workgroup_size: 256
    .name:           _Z9deconv3_kPKDF16_PKfS2_Pf
    .private_segment_fixed_size: 0
    .sgpr_count:     26
    .sgpr_spill_count: 0
    .symbol:         _Z9deconv3_kPKDF16_PKfS2_Pf.kd
    .uniform_work_group_size: 1
    .uses_dynamic_stack: false
    .vgpr_count:     55
    .vgpr_spill_count: 0
    .wavefront_size: 64
  - .agpr_count:     8
    .args:
      - .offset:         0
        .size:           112
        .value_kind:     by_value
    .group_segment_fixed_size: 49152
    .kernarg_segment_align: 8
    .kernarg_segment_size: 112
    .language:       OpenCL C
    .language_version:
      - 2
      - 0
    .max_flat_workgroup_size: 256
    .name:           _Z6gemm_gILi32ELi64ELi16ELi32ELi1ELi0ELi64ELi4EEv5GemmP
    .private_segment_fixed_size: 0
    .sgpr_count:     34
    .sgpr_spill_count: 0
    .symbol:         _Z6gemm_gILi32ELi64ELi16ELi32ELi1ELi0ELi64ELi4EEv5GemmP.kd
    .uniform_work_group_size: 1
    .uses_dynamic_stack: false
    .vgpr_count:     40
    .vgpr_spill_count: 0
    .wavefront_size: 64
  - .agpr_count:     16
    .args:
      - .offset:         0
        .size:           112
        .value_kind:     by_value
    .group_segment_fixed_size: 65536
    .kernarg_segment_align: 8
    .kernarg_segment_size: 112
    .language:       OpenCL C
    .language_version:
      - 2
      - 0
    .max_flat_workgroup_size: 256
    .name:           _Z6gemm_gILi64ELi64ELi32ELi32ELi1ELi0ELi64ELi4EEv5GemmP
    .private_segment_fixed_size: 0
    .sgpr_count:     34
    .sgpr_spill_count: 0
    .symbol:         _Z6gemm_gILi64ELi64ELi32ELi32ELi1ELi0ELi64ELi4EEv5GemmP.kd
    .uniform_work_group_size: 1
    .uses_dynamic_stack: false
    .vgpr_count:     56
    .vgpr_spill_count: 0
    .wavefront_size: 64
  - .agpr_count:     32
    .args:
      - .offset:         0
        .size:           112
        .value_kind:     by_value
    .group_segment_fixed_size: 73728
    .kernarg_segment_align: 8
    .kernarg_segment_size: 112
    .language:       OpenCL C
    .language_version:
      - 2
      - 0
    .max_flat_workgroup_size: 256
    .name:           _Z6gemm_gILi64ELi128ELi32ELi64ELi0ELi2ELi64ELi3EEv5GemmP
    .private_segment_fixed_size: 0
    .sgpr_count:     27
    .sgpr_spill_count: 0
    .symbol:         _Z6gemm_gILi64ELi128ELi32ELi64ELi0ELi2ELi64ELi3EEv5GemmP.kd
    .uniform_work_group_size: 1
    .uses_dynamic_stack: false
    .vgpr_count:     80
    .vgpr_spill_count: 0
    .wavefront_size: 64
  - .agpr_count:     16
    .args:
      - .offset:         0
        .size:           112
        .value_kind:     by_value
    .group_segment_fixed_size: 49152
    .kernarg_segment_align: 8
    .kernarg_segment_size: 112
    .language:       OpenCL C
    .language_version:
      - 2
      - 0
    .max_flat_workgroup_size: 256
    .name:           _Z6gemm_gILi64ELi64ELi32ELi32ELi0ELi3ELi64ELi3EEv5GemmP
    .private_segment_fixed_size: 0
    .sgpr_count:     30
    .sgpr_spill_count: 0
    .symbol:         _Z6gemm_gILi64ELi64ELi32ELi32ELi0ELi3ELi64ELi3EEv5GemmP.kd
    .uniform_work_group_size: 1
    .uses_dynamic_stack: false
    .vgpr_count:     56
    .vgpr_spill_count: 0
    .wavefront_size: 64
  - .agpr_count:     16
    .args:
      - .offset:         0
        .size:           112
        .value_kind:     by_value
    .group_segment_fixed_size: 49152
    .kernarg_segment_align: 8
    .kernarg_segment_size: 112
    .language:       OpenCL C
    .language_version:
      - 2
      - 0
    .max_flat_workgroup_size: 256
    .name:           _Z6gemm_gILi64ELi64ELi32ELi32ELi0ELi4ELi64ELi3EEv5GemmP
    .private_segment_fixed_size: 0
    .sgpr_count:     27
    .sgpr_spill_count: 0
    .symbol:         _Z6gemm_gILi64ELi64ELi32ELi32ELi0ELi4ELi64ELi3EEv5GemmP.kd
    .uniform_work_group_size: 1
    .uses_dynamic_stack: false
    .vgpr_count:     52
    .vgpr_spill_count: 0
    .wavefront_size: 64
  - .agpr_count:     8
    .args:
      - .offset:         0
        .size:           112
        .value_kind:     by_value
    .group_segment_fixed_size: 73728
    .kernarg_segment_align: 8
    .kernarg_segment_size: 112
    .language:       OpenCL C
    .language_version:
      - 2
      - 0
    .max_flat_workgroup_size: 256
    .name:           _Z6gemm_gILi32ELi64ELi16ELi32ELi1ELi1ELi128ELi3EEv5GemmP
    .private_segment_fixed_size: 0
    .sgpr_count:     38
    .sgpr_spill_count: 0
    .symbol:         _Z6gemm_gILi32ELi64ELi16ELi32ELi1ELi1ELi128ELi3EEv5GemmP.kd
    .uniform_work_group_size: 1
    .uses_dynamic_stack: false
    .vgpr_count:     48
    .vgpr_spill_count: 0
    .wavefront_size: 64
  - .agpr_count:     8
    .args:
      - .offset:         0
        .size:           112
        .value_kind:     by_value
    .group_segment_fixed_size: 49152
    .kernarg_segment_align: 8
    .kernarg_segment_size: 112
    .language:       OpenCL C
    .language_version:
      - 2
      - 0
    .max_flat_workgroup_size: 256
    .name:           _Z6gemm_gILi32ELi64ELi16ELi32ELi1ELi1ELi64ELi4EEv5GemmP
    .private_segment_fixed_size: 0
    .sgpr_count:     36
    .sgpr_spill_count: 0
    .symbol:         _Z6gemm_gILi32ELi64ELi16ELi32ELi1ELi1ELi64ELi4EEv5GemmP.kd
    .uniform_work_group_size: 1
    .uses_dynamic_stack: false
    .vgpr_count:     40
    .vgpr_spill_count: 0
    .wavefront_size: 64
